# P0 router-weight preparation: all 8 weight/gain pairs of an entry loaded up front with one wait instead of 8 serial load-wait round trips
# baseline (speedup 1.0000x reference)
; __device__ __forceinline__ unsigned f2bf(float f) { unsigned u = __builtin_bit_cast(unsigned, f); return (u + 0x7fffu + ((u >> 16) & 1u)) >> 16; }
; __device__ __forceinline__ void p0_prologue(Frame& F) {
;     ...
;     { u32x4* wrb = WSP(u32x4, WS_WRG);
;       for (int i = F.vcu * NTHREADS + F.tid; i < 32 * 4 * 2 * 64; i += F.G * NTHREADS) {
;           const int ln = i & 63, pc = (i >> 6) & 1, j = (i >> 7) & 3, c = i >> 9;
;           const int k0 = 64 * c + 32 * (ln >> 5) + 8 * j, n = ln & 31;
;           unsigned hw[8];
; #pragma unroll
;           for (int t = 0; t < 8; ++t) { const float w = F.w_router[(size_t)(k0 + t) * NE + n] * F.g_moe[k0 + t]; const unsigned hi = f2bf(w); const float rest = w - __builtin_bit_cast(float, hi << 16); hw[t] = pc ? f2bf(rest) : hi; }
;           wrb[i] = (u32x4){hw[0] | (hw[1] << 16), hw[2] | (hw[3] << 16), hw[4] | (hw[5] << 16), hw[6] | (hw[7] << 16)}; } }
.LBB0_105:
	v_ashrrev_i32_e32 v1, 3, v6
	v_lshrrev_b32_e32 v8, 4, v6
	v_and_b32_e32 v1, 0xffffffc0, v1
	v_and_b32_e32 v7, 32, v6
	v_and_b32_e32 v8, 24, v8
	v_or3_b32 v8, v1, v7, v8
	v_ashrrev_i32_e32 v9, 31, v8
	v_lshlrev_b64 v[10:11], 7, v[8:9]
	v_readlane_b32 s36, v254, 11
	v_readlane_b32 s44, v254, 19
	v_readlane_b32 s45, v254, 20
	v_readlane_b32 s37, v254, 12
	v_readlane_b32 s38, v254, 13
	v_readlane_b32 s39, v254, 14
	v_readlane_b32 s40, v254, 15
	v_readlane_b32 s41, v254, 16
	v_readlane_b32 s42, v254, 17
	v_readlane_b32 s43, v254, 18
	v_readlane_b32 s46, v254, 21
	v_readlane_b32 s47, v254, 22
	v_readlane_b32 s48, v254, 23
	v_readlane_b32 s49, v254, 24
	v_readlane_b32 s50, v254, 25
	v_readlane_b32 s51, v254, 26
	v_lshl_add_u64 v[10:11], v[2:3], 0, v[10:11]
	v_lshl_add_u64 v[12:13], v[8:9], 2, s[44:45]
	global_load_dword v200, v[10:11], off
	global_load_dword v201, v[10:11], off offset:128
	global_load_dword v202, v[10:11], off offset:256
	global_load_dword v203, v[10:11], off offset:384
	global_load_dword v204, v[10:11], off offset:512
	global_load_dword v205, v[10:11], off offset:640
	global_load_dword v206, v[10:11], off offset:768
	global_load_dword v207, v[10:11], off offset:896
	global_load_dwordx4 v[208:211], v[12:13], off
	global_load_dwordx4 v[212:215], v[12:13], off offset:16
	v_and_b32_e32 v9, 64, v6
	v_cmp_ne_u32_e32 vcc, 0, v9
	s_waitcnt vmcnt(0)
	v_mul_f32_e32 v200, v200, v208
	v_mul_f32_e32 v201, v201, v209
	v_mul_f32_e32 v202, v202, v210
	v_mul_f32_e32 v203, v203, v211
	v_mul_f32_e32 v204, v204, v212
	v_mul_f32_e32 v205, v205, v213
	v_mul_f32_e32 v206, v206, v214
	v_mul_f32_e32 v207, v207, v215
	v_bfe_u32 v1, v200, 16, 1
	v_add3_u32 v1, v200, v1, s3
	v_bfe_u32 v7, v201, 16, 1
	v_add3_u32 v7, v201, v7, s3
	v_bfe_u32 v9, v202, 16, 1
	v_add3_u32 v9, v202, v9, s3
	v_bfe_u32 v12, v203, 16, 1
	v_add3_u32 v12, v203, v12, s3
	v_bfe_u32 v13, v204, 16, 1
	v_add3_u32 v13, v204, v13, s3
	v_bfe_u32 v14, v205, 16, 1
	v_add3_u32 v14, v205, v14, s3
	v_bfe_u32 v15, v206, 16, 1
	v_add3_u32 v15, v206, v15, s3
	v_bfe_u32 v8, v207, 16, 1
	v_add3_u32 v8, v207, v8, s3
	s_and_saveexec_b64 s[10:11], vcc
	v_and_b32_e32 v1, 0xffff0000, v1
	v_sub_f32_e32 v1, v200, v1
	v_bfe_u32 v16, v1, 16, 1
	v_add3_u32 v1, v1, v16, s3
	v_and_b32_e32 v7, 0xffff0000, v7
	v_sub_f32_e32 v7, v201, v7
	v_bfe_u32 v16, v7, 16, 1
	v_add3_u32 v7, v7, v16, s3
	v_and_b32_e32 v9, 0xffff0000, v9
	v_sub_f32_e32 v9, v202, v9
	v_bfe_u32 v16, v9, 16, 1
	v_add3_u32 v9, v9, v16, s3
	v_and_b32_e32 v12, 0xffff0000, v12
	v_sub_f32_e32 v12, v203, v12
	v_bfe_u32 v16, v12, 16, 1
	v_add3_u32 v12, v12, v16, s3
	v_and_b32_e32 v13, 0xffff0000, v13
	v_sub_f32_e32 v13, v204, v13
	v_bfe_u32 v16, v13, 16, 1
	v_add3_u32 v13, v13, v16, s3
	v_and_b32_e32 v14, 0xffff0000, v14
	v_sub_f32_e32 v14, v205, v14
	v_bfe_u32 v16, v14, 16, 1
	v_add3_u32 v14, v14, v16, s3
	v_and_b32_e32 v15, 0xffff0000, v15
	v_sub_f32_e32 v15, v206, v15
	v_bfe_u32 v16, v15, 16, 1
	v_add3_u32 v15, v15, v16, s3
	v_and_b32_e32 v8, 0xffff0000, v8
	v_sub_f32_e32 v8, v207, v8
	v_bfe_u32 v16, v8, 16, 1
	v_add3_u32 v8, v8, v16, s3
	s_branch .LBB0_104
